# K-loop touch loads warm the next GEMM's weight operand in the Infinity Cache (P7 -> w_out for P9, P9 -> peer_w_q for P11)
# speedup vs baseline: 1.0114x; 1.0069x over previous
.LBB0_1024:
	ds_read_b128 v[146:149], v225
	ds_read_b128 v[150:153], v225 offset:1024
	ds_read_b128 v[154:157], v225 offset:2048
	ds_read_b128 v[158:161], v225 offset:3072
	ds_read_b128 v[62:65], v226
	ds_read_b128 v[66:69], v226 offset:1024
	ds_read_b128 v[138:141], v226 offset:2048
	ds_read_b128 v[142:145], v226 offset:3072
	s_cmp_eq_u32 s42, 0
	s_cselect_b64 s[44:45], -1, 0
	v_lshl_add_u64 v[216:217], v[212:213], 0, s[42:43]
	s_add_i32 m0, s37, 0xc000
	ds_read_b128 v[186:189], v227
	ds_read_b128 v[190:193], v227 offset:1024
	ds_read_b128 v[178:181], v227 offset:2048
	ds_read_b128 v[182:185], v227 offset:3072
	ds_read_b128 v[170:173], v227 offset:4096
	ds_read_b128 v[174:177], v227 offset:5120
	ds_read_b128 v[162:165], v227 offset:6144
	ds_read_b128 v[166:169], v227 offset:7168
	global_load_lds_dwordx4 v[216:217], off
	v_lshl_add_u64 v[216:217], v[214:215], 0, s[42:43]
	s_add_i32 m0, s37, 0xe000
	s_and_b64 s[44:45], s[40:41], s[44:45]
	global_load_lds_dwordx4 v[216:217], off
	s_cmpk_lg_u32 s42, 0x200
	s_cbranch_scc1 .Lwarm7_skip
	v_lshl_or_b32 v246, s84, 9, v0
	v_lshlrev_b32_e32 v246, 7, v246
	s_add_u32 s76, s88, 0x9c00000
	s_addc_u32 s77, s89, 0
	global_load_dword v247, v246, s[76:77]
.Lwarm7_skip:
	s_and_b64 vcc, exec, s[44:45]
	s_cbranch_vccnz .LBB0_1026
	s_waitcnt vmcnt(8)

.LBB0_1182:
	ds_read_b128 v[146:149], v225
	ds_read_b128 v[150:153], v225 offset:1024
	ds_read_b128 v[154:157], v225 offset:2048
	ds_read_b128 v[158:161], v225 offset:3072
	ds_read_b128 v[106:109], v226
	ds_read_b128 v[110:113], v226 offset:1024
	ds_read_b128 v[122:125], v226 offset:2048
	ds_read_b128 v[126:129], v226 offset:3072
	s_cmp_eq_u32 s34, 0
	s_cselect_b64 s[36:37], -1, 0
	v_lshl_add_u64 v[216:217], v[212:213], 0, s[34:35]
	s_add_i32 m0, s27, 0xc000
	ds_read_b128 v[186:189], v227
	ds_read_b128 v[190:193], v227 offset:1024
	ds_read_b128 v[178:181], v227 offset:2048
	ds_read_b128 v[182:185], v227 offset:3072
	ds_read_b128 v[170:173], v227 offset:4096
	ds_read_b128 v[174:177], v227 offset:5120
	ds_read_b128 v[162:165], v227 offset:6144
	ds_read_b128 v[166:169], v227 offset:7168
	global_load_lds_dwordx4 v[216:217], off
	v_lshl_add_u64 v[216:217], v[214:215], 0, s[34:35]
	s_add_i32 m0, s27, 0xe000
	s_and_b64 s[36:37], s[30:31], s[36:37]
	global_load_lds_dwordx4 v[216:217], off
	s_cmpk_lg_u32 s34, 0x200
	s_cbranch_scc1 .Lwarm9_skip
	v_and_b32_e32 v246, 0xff, v0
	v_lshl_or_b32 v246, s84, 8, v246
	v_lshlrev_b32_e32 v246, 7, v246
	s_add_u32 s66, s88, 0xbc00000
	s_addc_u32 s67, s89, 0
	global_load_dword v247, v246, s[66:67]
